# residual-add GEMM epilogues (out-proj, FFN down, pool mixer): residual loads batched ahead of the adds and stores instead of one row group at a time
# baseline (speedup 1.0000x reference)
; #define PG8_STAGE(bufoff, gbase, voff) do { _Pragma("unroll") for (int _i = 0; _i < 2; ++_i) glds16_s((const void*)((const char*)(gbase) + _i * r64), (voff), ldsb + (unsigned)(bufoff) + ldsw + _i * 8192u); } while (0)
; #define PG8_LDA(b, h) do { _Pragma("unroll") for (int m = 0; m < 4; ++m) { const int o_ = PG8_SA(b, h) + aoff + m * 2048; \
;         if constexpr (FP8) A8[m] = PG8_CAT8(o_); else { At[m][0] = PG8_LD16(o_); At[m][1] = PG8_LD16(o_ + 1024); } } } while (0)
; #define PG8_LDB(X, X8, b, h) do { _Pragma("unroll") for (int n = 0; n < 2; ++n) { const int o_ = PG8_SB(b, h) + boff + n * 2048; \
;         if constexpr (FP8) X8[n] = PG8_CAT8(o_); else { X[n][0] = PG8_LD16(o_); X[n][1] = PG8_LD16(o_ + 1024); } } } while (0)
; #define PG8_WAIT_V(n) asm volatile("s_waitcnt vmcnt(" #n ")" ::: "memory")
; #define PG8_WAIT_L(n) asm volatile("s_waitcnt lgkmcnt(" #n ")" ::: "memory")
; #define PG8_BAR __builtin_amdgcn_s_barrier()
; #define PG8_SCHED __builtin_amdgcn_sched_barrier(0)
; #define PG8_HI do { if constexpr (FP8) asm volatile("s_setprio 1"); } while (0)
; #define PG8_LO do { if constexpr (FP8) asm volatile("s_setprio 0"); } while (0)
; template <class Epi, class Sched, bool FP8 = false>
; __device__ __forceinline__ void gemm_phase(LAS unsigned char* lds, const int Kb, const int nt  , const Sched& S, const Epi& E) {
;     ...
;             PG8_LDB(B0, B08, 0, 0); PG8_SCHED; PG8_LDA(0, 0); PG8_STAGE(PG8_SA(1, 1), a1 + hstep, voffA);
;             PG8_WAIT_L(8); PG8_BAR; PG8_HI; PG8_WAIT_L(0); PG8_MMA(0, 0, B0, B08); PG8_BAR; PG8_LO; PG8_SCHED;
;             PG8_LDB(B1, B18, 0, 1); PG8_STAGE(PG8_SB(0, 0), b2, voffB);
;             PG8_BAR; PG8_HI; PG8_WAIT_L(0); PG8_MMA(0, 1, B1, B18); PG8_BAR; PG8_LO;
;             PG8_LDA(0, 1); PG8_STAGE(PG8_SA(0, 0), a2, voffA);
;             PG8_BAR; PG8_HI; PG8_WAIT_L(0); PG8_MMA(1, 0, B0, B08); PG8_BAR; PG8_LO; PG8_SCHED;
;             PG8_STAGE(PG8_SB(0, 1), b2 + hstep, voffB);
;             PG8_WAIT_V(6); PG8_BAR; PG8_HI; PG8_MMA(1, 1, B1, B18); PG8_BAR; PG8_LO;
.LBB0_2043:
	ds_read_b128 v[150:153], v132
	ds_read_b128 v[154:157], v133
	ds_read_b128 v[158:161], v134
	ds_read_b128 v[162:165], v135
	s_add_u32 s22, s20, 0xffea0080
	s_addc_u32 s23, s21, -1
	s_cmpk_eq_i32 s59, 0x54
	s_cselect_b32 s24, s16, s22
	s_cselect_b32 s25, s17, s23
	s_cselect_b32 s22, s18, s57
	s_cselect_b32 s23, s19, s58
	s_add_u32 s26, s24, 0x80
	s_addc_u32 s27, s25, 0
	ds_read_b128 v[166:169], v148
	ds_read_b128 v[170:173], v148 offset:1024
	ds_read_b128 v[174:177], v148 offset:2048
	ds_read_b128 v[178:181], v148 offset:3072
	ds_read_b128 v[182:185], v148 offset:4096
	ds_read_b128 v[186:189], v148 offset:5120
	ds_read_b128 v[194:197], v148 offset:6144
	ds_read_b128 v[198:201], v148 offset:7168
	s_mov_b32 s60, m0
	s_mov_b32 m0, s51
	s_nop 0
	global_load_lds_dwordx4 v1, s[20:21]
	s_mov_b32 m0, s60
	s_add_u32 s60, s20, 0xb0000
	s_addc_u32 s61, s21, 0
	s_mov_b32 s62, m0
	s_mov_b32 m0, s52
	s_nop 0
	global_load_lds_dwordx4 v1, s[60:61]
	s_mov_b32 m0, s62
	s_waitcnt lgkmcnt(8)
	s_barrier
	s_waitcnt lgkmcnt(0)
	s_setprio 1
	v_mfma_f32_16x16x32_bf16 v[126:129], v[150:153], v[166:169], v[126:129]
	v_mfma_f32_16x16x32_bf16 v[122:125], v[158:161], v[166:169], v[122:125]
	v_mfma_f32_16x16x32_bf16 v[110:113], v[150:153], v[174:177], v[110:113]
	v_mfma_f32_16x16x32_bf16 v[106:109], v[158:161], v[174:177], v[106:109]
	v_mfma_f32_16x16x32_bf16 v[94:97], v[150:153], v[182:185], v[94:97]
	v_mfma_f32_16x16x32_bf16 v[90:93], v[158:161], v[182:185], v[90:93]
	v_mfma_f32_16x16x32_bf16 v[78:81], v[150:153], v[194:197], v[78:81]
	v_mfma_f32_16x16x32_bf16 v[74:77], v[158:161], v[194:197], v[74:77]
	v_mfma_f32_16x16x32_bf16 v[126:129], v[154:157], v[170:173], v[126:129]
	v_mfma_f32_16x16x32_bf16 v[122:125], v[162:165], v[170:173], v[122:125]
	v_mfma_f32_16x16x32_bf16 v[110:113], v[154:157], v[178:181], v[110:113]
	v_mfma_f32_16x16x32_bf16 v[106:109], v[162:165], v[178:181], v[106:109]
	v_mfma_f32_16x16x32_bf16 v[94:97], v[154:157], v[186:189], v[94:97]
	v_mfma_f32_16x16x32_bf16 v[90:93], v[162:165], v[186:189], v[90:93]
	v_mfma_f32_16x16x32_bf16 v[78:81], v[154:157], v[198:201], v[78:81]
	v_mfma_f32_16x16x32_bf16 v[74:77], v[162:165], v[198:201], v[74:77]
	s_setprio 0
	s_barrier
	ds_read_b128 v[202:205], v136
	ds_read_b128 v[206:209], v137
	ds_read_b128 v[210:213], v138
	ds_read_b128 v[214:217], v139
	s_mov_b32 s60, m0
	s_mov_b32 m0, s36
	s_nop 0
	global_load_lds_dwordx4 v1, s[22:23]
	s_mov_b32 m0, s60
	s_add_u32 s60, s22, 0xb0000
	s_addc_u32 s61, s23, 0
	s_mov_b32 s62, m0
	s_mov_b32 m0, s37
	s_nop 0
	global_load_lds_dwordx4 v1, s[60:61]
	s_mov_b32 m0, s62
	s_barrier
	s_waitcnt lgkmcnt(0)
	s_setprio 1
	v_mfma_f32_16x16x32_bf16 v[118:121], v[202:205], v[166:169], v[118:121]
	v_mfma_f32_16x16x32_bf16 v[114:117], v[210:213], v[166:169], v[114:117]
	v_mfma_f32_16x16x32_bf16 v[102:105], v[202:205], v[174:177], v[102:105]
	v_mfma_f32_16x16x32_bf16 v[98:101], v[210:213], v[174:177], v[98:101]
	v_mfma_f32_16x16x32_bf16 v[86:89], v[202:205], v[182:185], v[86:89]
	v_mfma_f32_16x16x32_bf16 v[82:85], v[210:213], v[182:185], v[82:85]
	v_mfma_f32_16x16x32_bf16 v[70:73], v[202:205], v[194:197], v[70:73]
	v_mfma_f32_16x16x32_bf16 v[66:69], v[210:213], v[194:197], v[66:69]
	v_mfma_f32_16x16x32_bf16 v[118:121], v[206:209], v[170:173], v[118:121]
	v_mfma_f32_16x16x32_bf16 v[114:117], v[214:217], v[170:173], v[114:117]
	v_mfma_f32_16x16x32_bf16 v[102:105], v[206:209], v[178:181], v[102:105]
	v_mfma_f32_16x16x32_bf16 v[98:101], v[214:217], v[178:181], v[98:101]
	v_mfma_f32_16x16x32_bf16 v[86:89], v[206:209], v[186:189], v[86:89]
	v_mfma_f32_16x16x32_bf16 v[82:85], v[214:217], v[186:189], v[82:85]
	v_mfma_f32_16x16x32_bf16 v[70:73], v[206:209], v[198:201], v[70:73]
	v_mfma_f32_16x16x32_bf16 v[66:69], v[214:217], v[198:201], v[66:69]
	s_setprio 0
	s_barrier
	ds_read_b128 v[166:169], v148 offset:16384
	ds_read_b128 v[170:173], v148 offset:17408
	ds_read_b128 v[174:177], v148 offset:18432
	ds_read_b128 v[178:181], v148 offset:19456
	ds_read_b128 v[182:185], v148 offset:20480
	ds_read_b128 v[186:189], v148 offset:21504
	ds_read_b128 v[194:197], v148 offset:22528
	ds_read_b128 v[198:201], v148 offset:23552
	s_mov_b32 s60, m0
	s_mov_b32 m0, s35
	s_nop 0
	global_load_lds_dwordx4 v1, s[24:25]
	s_mov_b32 m0, s60
	s_add_u32 s60, s24, 0xb0000
	s_addc_u32 s61, s25, 0
	s_mov_b32 s62, m0
	s_mov_b32 m0, s38
	s_nop 0
	global_load_lds_dwordx4 v1, s[60:61]
	s_mov_b32 m0, s62
	s_barrier
	s_waitcnt lgkmcnt(0)
	s_setprio 1
	v_mfma_f32_16x16x32_bf16 v[62:65], v[150:153], v[166:169], v[62:65]
	v_mfma_f32_16x16x32_bf16 v[58:61], v[158:161], v[166:169], v[58:61]
	v_mfma_f32_16x16x32_bf16 v[46:49], v[150:153], v[174:177], v[46:49]
	v_mfma_f32_16x16x32_bf16 v[42:45], v[158:161], v[174:177], v[42:45]
	v_mfma_f32_16x16x32_bf16 v[30:33], v[150:153], v[182:185], v[30:33]
	v_mfma_f32_16x16x32_bf16 v[26:29], v[158:161], v[182:185], v[26:29]
	v_mfma_f32_16x16x32_bf16 v[14:17], v[150:153], v[194:197], v[14:17]
	v_mfma_f32_16x16x32_bf16 v[10:13], v[158:161], v[194:197], v[10:13]
	v_mfma_f32_16x16x32_bf16 v[62:65], v[154:157], v[170:173], v[62:65]
	v_mfma_f32_16x16x32_bf16 v[58:61], v[162:165], v[170:173], v[58:61]
	v_mfma_f32_16x16x32_bf16 v[46:49], v[154:157], v[178:181], v[46:49]
	v_mfma_f32_16x16x32_bf16 v[42:45], v[162:165], v[178:181], v[42:45]
	v_mfma_f32_16x16x32_bf16 v[30:33], v[154:157], v[186:189], v[30:33]
	v_mfma_f32_16x16x32_bf16 v[26:29], v[162:165], v[186:189], v[26:29]
	v_mfma_f32_16x16x32_bf16 v[14:17], v[154:157], v[198:201], v[14:17]
	v_mfma_f32_16x16x32_bf16 v[10:13], v[162:165], v[198:201], v[10:13]
	s_setprio 0
	s_barrier
; #define PG8_STAGE(bufoff, gbase, voff) do { _Pragma("unroll") for (int _i = 0; _i < 2; ++_i) glds16_s((const void*)((const char*)(gbase) + _i * r64), (voff), ldsb + (unsigned)(bufoff) + ldsw + _i * 8192u); } while (0)
; #define PG8_LDA(b, h) do { _Pragma("unroll") for (int m = 0; m < 4; ++m) { const int o_ = PG8_SA(b, h) + aoff + m * 2048; \
;         if constexpr (FP8) A8[m] = PG8_CAT8(o_); else { At[m][0] = PG8_LD16(o_); At[m][1] = PG8_LD16(o_ + 1024); } } } while (0)
; #define PG8_LDB(X, X8, b, h) do { _Pragma("unroll") for (int n = 0; n < 2; ++n) { const int o_ = PG8_SB(b, h) + boff + n * 2048; \
;         if constexpr (FP8) X8[n] = PG8_CAT8(o_); else { X[n][0] = PG8_LD16(o_); X[n][1] = PG8_LD16(o_ + 1024); } } } while (0)
; #define PG8_WAIT_V(n) asm volatile("s_waitcnt vmcnt(" #n ")" ::: "memory")
; #define PG8_WAIT_L(n) asm volatile("s_waitcnt lgkmcnt(" #n ")" ::: "memory")
; #define PG8_BAR __builtin_amdgcn_s_barrier()
; #define PG8_SCHED __builtin_amdgcn_sched_barrier(0)
; #define PG8_HI do { if constexpr (FP8) asm volatile("s_setprio 1"); } while (0)
; #define PG8_LO do { if constexpr (FP8) asm volatile("s_setprio 0"); } while (0)
; template <class Epi, class Sched, bool FP8 = false>
; __device__ __forceinline__ void gemm_phase(LAS unsigned char* lds, const int Kb, const int nt  , const Sched& S, const Epi& E) {
;     ...
;             PG8_WAIT_V(6); PG8_BAR; PG8_HI; PG8_MMA(1, 1, B1, B18); PG8_BAR; PG8_LO;
;             PG8_LDB(B0, B08, 1, 0); PG8_SCHED; PG8_LDA(1, 0); PG8_STAGE(PG8_SA(0, 1), a2 + hstep, voffA);
;             PG8_WAIT_L(8); PG8_BAR; PG8_HI; PG8_WAIT_L(0); PG8_MMA(0, 0, B0, B08); PG8_BAR; PG8_LO; PG8_SCHED;
;             PG8_LDB(B1, B18, 1, 1); PG8_STAGE(PG8_SB(1, 0), b3, voffB);
;             PG8_BAR; PG8_HI; PG8_WAIT_L(0); PG8_MMA(0, 1, B1, B18); PG8_BAR; PG8_LO;
;             PG8_LDA(1, 1); PG8_STAGE(PG8_SA(1, 0), a3, voffA);
;             PG8_BAR; PG8_HI; PG8_WAIT_L(0); PG8_MMA(1, 0, B0, B08); PG8_BAR; PG8_LO; PG8_SCHED;
	s_add_u32 s60, s22, 0x160000
	s_addc_u32 s61, s23, 0
	s_mov_b32 s62, m0
	s_mov_b32 m0, s39
	s_nop 0
	global_load_lds_dwordx4 v1, s[60:61]
	s_mov_b32 m0, s62
	s_add_u32 s60, s22, 0x210000
	s_addc_u32 s61, s23, 0
	s_mov_b32 s62, m0
	s_mov_b32 m0, s40
	s_nop 0
	global_load_lds_dwordx4 v1, s[60:61]
	s_mov_b32 m0, s62
	s_waitcnt vmcnt(6)
	s_barrier
	s_setprio 1
	v_mfma_f32_16x16x32_bf16 v[54:57], v[202:205], v[166:169], v[54:57]
	v_mfma_f32_16x16x32_bf16 v[50:53], v[210:213], v[166:169], v[50:53]
	v_mfma_f32_16x16x32_bf16 v[38:41], v[202:205], v[174:177], v[38:41]
	v_mfma_f32_16x16x32_bf16 v[34:37], v[210:213], v[174:177], v[34:37]
	v_mfma_f32_16x16x32_bf16 v[22:25], v[202:205], v[182:185], v[22:25]
	v_mfma_f32_16x16x32_bf16 v[18:21], v[210:213], v[182:185], v[18:21]
	v_mfma_f32_16x16x32_bf16 v[6:9], v[202:205], v[194:197], v[6:9]
	v_mfma_f32_16x16x32_bf16 v[2:5], v[210:213], v[194:197], v[2:5]
	v_mfma_f32_16x16x32_bf16 v[54:57], v[206:209], v[170:173], v[54:57]
	v_mfma_f32_16x16x32_bf16 v[50:53], v[214:217], v[170:173], v[50:53]
	v_mfma_f32_16x16x32_bf16 v[38:41], v[206:209], v[178:181], v[38:41]
	v_mfma_f32_16x16x32_bf16 v[34:37], v[214:217], v[178:181], v[34:37]
	v_mfma_f32_16x16x32_bf16 v[22:25], v[206:209], v[186:189], v[22:25]
	v_mfma_f32_16x16x32_bf16 v[18:21], v[214:217], v[186:189], v[18:21]
	v_mfma_f32_16x16x32_bf16 v[6:9], v[206:209], v[198:201], v[6:9]
	v_mfma_f32_16x16x32_bf16 v[2:5], v[214:217], v[198:201], v[2:5]
	s_setprio 0
	s_barrier
	ds_read_b128 v[150:153], v140
	ds_read_b128 v[154:157], v141
	ds_read_b128 v[158:161], v142
	ds_read_b128 v[162:165], v143
	ds_read_b128 v[166:169], v148 offset:32768
	ds_read_b128 v[170:173], v148 offset:33792
	ds_read_b128 v[174:177], v148 offset:34816
	ds_read_b128 v[178:181], v148 offset:35840
	ds_read_b128 v[182:185], v148 offset:36864
	ds_read_b128 v[186:189], v148 offset:37888
	ds_read_b128 v[194:197], v148 offset:38912
	ds_read_b128 v[198:201], v148 offset:39936
	s_add_u32 s60, s24, 0x160000
	s_addc_u32 s61, s25, 0
	s_mov_b32 s62, m0
	s_mov_b32 m0, s41
	s_nop 0
	global_load_lds_dwordx4 v1, s[60:61]
	s_mov_b32 m0, s62
	s_add_u32 s60, s24, 0x210000
	s_addc_u32 s61, s25, 0
	s_mov_b32 s62, m0
	s_mov_b32 m0, s42
	s_nop 0
	global_load_lds_dwordx4 v1, s[60:61]
	s_mov_b32 m0, s62
	s_waitcnt lgkmcnt(8)
	s_barrier
	s_waitcnt lgkmcnt(0)
	s_setprio 1
	v_mfma_f32_16x16x32_bf16 v[126:129], v[150:153], v[166:169], v[126:129]
	v_mfma_f32_16x16x32_bf16 v[122:125], v[158:161], v[166:169], v[122:125]
	v_mfma_f32_16x16x32_bf16 v[110:113], v[150:153], v[174:177], v[110:113]
	v_mfma_f32_16x16x32_bf16 v[106:109], v[158:161], v[174:177], v[106:109]
	v_mfma_f32_16x16x32_bf16 v[94:97], v[150:153], v[182:185], v[94:97]
	v_mfma_f32_16x16x32_bf16 v[90:93], v[158:161], v[182:185], v[90:93]
	v_mfma_f32_16x16x32_bf16 v[78:81], v[150:153], v[194:197], v[78:81]
	v_mfma_f32_16x16x32_bf16 v[74:77], v[158:161], v[194:197], v[74:77]
	v_mfma_f32_16x16x32_bf16 v[126:129], v[154:157], v[170:173], v[126:129]
	v_mfma_f32_16x16x32_bf16 v[122:125], v[162:165], v[170:173], v[122:125]
	v_mfma_f32_16x16x32_bf16 v[110:113], v[154:157], v[178:181], v[110:113]
	v_mfma_f32_16x16x32_bf16 v[106:109], v[162:165], v[178:181], v[106:109]
	v_mfma_f32_16x16x32_bf16 v[94:97], v[154:157], v[186:189], v[94:97]
	v_mfma_f32_16x16x32_bf16 v[90:93], v[162:165], v[186:189], v[90:93]
	v_mfma_f32_16x16x32_bf16 v[78:81], v[154:157], v[198:201], v[78:81]
	v_mfma_f32_16x16x32_bf16 v[74:77], v[162:165], v[198:201], v[74:77]
	s_setprio 0
	s_barrier
	ds_read_b128 v[202:205], v144
	ds_read_b128 v[206:209], v145
	ds_read_b128 v[210:213], v146
	ds_read_b128 v[214:217], v147
	s_add_u32 s60, s22, 0x80
	s_addc_u32 s61, s23, 0
	s_mov_b32 s62, m0
	s_mov_b32 m0, s45
	s_nop 0
	global_load_lds_dwordx4 v1, s[60:61]
	s_mov_b32 m0, s62
	s_add_u32 s60, s22, 0xb0080
	s_addc_u32 s61, s23, 0
	s_mov_b32 s62, m0
	s_mov_b32 m0, s46
	s_nop 0
	global_load_lds_dwordx4 v1, s[60:61]
	s_mov_b32 m0, s62
	s_barrier
	s_waitcnt lgkmcnt(0)
	s_setprio 1
	v_mfma_f32_16x16x32_bf16 v[118:121], v[202:205], v[166:169], v[118:121]
	v_mfma_f32_16x16x32_bf16 v[114:117], v[210:213], v[166:169], v[114:117]
	v_mfma_f32_16x16x32_bf16 v[102:105], v[202:205], v[174:177], v[102:105]
	v_mfma_f32_16x16x32_bf16 v[98:101], v[210:213], v[174:177], v[98:101]
	v_mfma_f32_16x16x32_bf16 v[86:89], v[202:205], v[182:185], v[86:89]
	v_mfma_f32_16x16x32_bf16 v[82:85], v[210:213], v[182:185], v[82:85]
	v_mfma_f32_16x16x32_bf16 v[70:73], v[202:205], v[194:197], v[70:73]
	v_mfma_f32_16x16x32_bf16 v[66:69], v[210:213], v[194:197], v[66:69]
	v_mfma_f32_16x16x32_bf16 v[118:121], v[206:209], v[170:173], v[118:121]
	v_mfma_f32_16x16x32_bf16 v[114:117], v[214:217], v[170:173], v[114:117]
	v_mfma_f32_16x16x32_bf16 v[102:105], v[206:209], v[178:181], v[102:105]
	v_mfma_f32_16x16x32_bf16 v[98:101], v[214:217], v[178:181], v[98:101]
	v_mfma_f32_16x16x32_bf16 v[86:89], v[206:209], v[186:189], v[86:89]
	v_mfma_f32_16x16x32_bf16 v[82:85], v[214:217], v[186:189], v[82:85]
	v_mfma_f32_16x16x32_bf16 v[70:73], v[206:209], v[198:201], v[70:73]
	v_mfma_f32_16x16x32_bf16 v[66:69], v[214:217], v[198:201], v[66:69]
	s_setprio 0
	s_barrier
	ds_read_b128 v[166:169], v148 offset:49152
	ds_read_b128 v[170:173], v148 offset:50176
	ds_read_b128 v[174:177], v148 offset:51200
	ds_read_b128 v[178:181], v148 offset:52224
	ds_read_b128 v[182:185], v148 offset:53248
	ds_read_b128 v[186:189], v148 offset:54272
	ds_read_b128 v[194:197], v148 offset:55296
	ds_read_b128 v[198:201], v148 offset:56320
	s_mov_b32 s60, m0
	s_mov_b32 m0, s47
	s_nop 0
	global_load_lds_dwordx4 v1, s[26:27]
	s_mov_b32 m0, s60
	s_add_u32 s24, s24, 0xb0080
	s_addc_u32 s25, s25, 0
	s_mov_b32 s26, m0
	s_mov_b32 m0, s48
	s_nop 0
	global_load_lds_dwordx4 v1, s[24:25]
	s_mov_b32 m0, s26
	s_barrier
; #define PG8_STAGE(bufoff, gbase, voff) do { _Pragma("unroll") for (int _i = 0; _i < 2; ++_i) glds16_s((const void*)((const char*)(gbase) + _i * r64), (voff), ldsb + (unsigned)(bufoff) + ldsw + _i * 8192u); } while (0)
; #define PG8_WAIT_V(n) asm volatile("s_waitcnt vmcnt(" #n ")" ::: "memory")
; #define PG8_WAIT_L(n) asm volatile("s_waitcnt lgkmcnt(" #n ")" ::: "memory")
; #define PG8_BAR __builtin_amdgcn_s_barrier()
; #define PG8_SCHED __builtin_amdgcn_sched_barrier(0)
; #define PG8_HI do { if constexpr (FP8) asm volatile("s_setprio 1"); } while (0)
; #define PG8_LO do { if constexpr (FP8) asm volatile("s_setprio 0"); } while (0)
;     __device__ __forceinline__ void operator()(const f32x4 (&acc)[2][2][4][2], const Unit& u, int wr, int wc, int fr, int fq) const {
;     ...
;         for (int ai = 0; ai < 2; ++ai)
; #pragma unroll
;             for (int m = 0; m < 4; ++m) { const size_t off = (size_t)(row0 + ai * HALF + m * 16) * ldc + col0;
; #pragma unroll
;                 for (int bj = 0; bj < 2; ++bj)
; #pragma unroll
;                     for (int n = 0; n < 2; ++n) { f32x4 v = acc[ai][bj][m][n] * cs[bj][n];
;                         if (res) v += *(const f32x4*)(res + off + bj * HALF + n * 16);
;                         *(f32x4*)(out + off + bj * HALF + n * 16) = v; }
;                 asm volatile("" ::: "memory"); }
; template <class Epi, class Sched, bool FP8 = false>
; __device__ __forceinline__ void gemm_phase(LAS unsigned char* lds, const int Kb, const int nt  , const Sched& S, const Epi& E) {
;     ...
;             PG8_BAR; PG8_HI; PG8_WAIT_L(0); PG8_MMA(1, 0, B0, B08); PG8_BAR; PG8_LO; PG8_SCHED;
;             PG8_STAGE(PG8_SB(1, 1), b3 + hstep, voffB);
;             PG8_WAIT_V(6); PG8_BAR; PG8_HI; PG8_MMA(1, 1, B1, B18); PG8_BAR; PG8_LO;
;         }
;         { int l_; asm volatile("v_mbcnt_lo_u32_b32 %0, -1, 0\n\tv_mbcnt_hi_u32_b32 %0, -1, %0" : "=v"(l_));
;           E(acc, cur, wr, wc, l_ & 15, l_ >> 4); }
	s_waitcnt lgkmcnt(0)
	s_setprio 1
	v_mfma_f32_16x16x32_bf16 v[62:65], v[150:153], v[166:169], v[62:65]
	v_mfma_f32_16x16x32_bf16 v[58:61], v[158:161], v[166:169], v[58:61]
	v_mfma_f32_16x16x32_bf16 v[46:49], v[150:153], v[174:177], v[46:49]
	v_mfma_f32_16x16x32_bf16 v[42:45], v[158:161], v[174:177], v[42:45]
	v_mfma_f32_16x16x32_bf16 v[30:33], v[150:153], v[182:185], v[30:33]
	v_mfma_f32_16x16x32_bf16 v[26:29], v[158:161], v[182:185], v[26:29]
	v_mfma_f32_16x16x32_bf16 v[14:17], v[150:153], v[194:197], v[14:17]
	v_mfma_f32_16x16x32_bf16 v[10:13], v[158:161], v[194:197], v[10:13]
	v_mfma_f32_16x16x32_bf16 v[62:65], v[154:157], v[170:173], v[62:65]
	v_mfma_f32_16x16x32_bf16 v[58:61], v[162:165], v[170:173], v[58:61]
	v_mfma_f32_16x16x32_bf16 v[46:49], v[154:157], v[178:181], v[46:49]
	v_mfma_f32_16x16x32_bf16 v[42:45], v[162:165], v[178:181], v[42:45]
	v_mfma_f32_16x16x32_bf16 v[30:33], v[154:157], v[186:189], v[30:33]
	v_mfma_f32_16x16x32_bf16 v[26:29], v[162:165], v[186:189], v[26:29]
	v_mfma_f32_16x16x32_bf16 v[14:17], v[154:157], v[198:201], v[14:17]
	v_mfma_f32_16x16x32_bf16 v[10:13], v[162:165], v[198:201], v[10:13]
	s_setprio 0
	s_barrier
	s_add_u32 s24, s22, 0x160080
	s_addc_u32 s25, s23, 0
	s_mov_b32 s26, m0
	s_mov_b32 m0, s49
	s_nop 0
	global_load_lds_dwordx4 v1, s[24:25]
	s_mov_b32 m0, s26
	s_add_u32 s22, s22, 0x210080
	s_addc_u32 s23, s23, 0
	s_mov_b32 s24, m0
	s_mov_b32 m0, s50
	s_nop 0
	global_load_lds_dwordx4 v1, s[22:23]
	s_mov_b32 m0, s24
	s_waitcnt vmcnt(6)
	s_barrier
	s_setprio 1
	v_mfma_f32_16x16x32_bf16 v[54:57], v[202:205], v[166:169], v[54:57]
	v_mfma_f32_16x16x32_bf16 v[50:53], v[210:213], v[166:169], v[50:53]
	v_mfma_f32_16x16x32_bf16 v[38:41], v[202:205], v[174:177], v[38:41]
	v_mfma_f32_16x16x32_bf16 v[34:37], v[210:213], v[174:177], v[34:37]
	v_mfma_f32_16x16x32_bf16 v[22:25], v[202:205], v[182:185], v[22:25]
	v_mfma_f32_16x16x32_bf16 v[18:21], v[210:213], v[182:185], v[18:21]
	v_mfma_f32_16x16x32_bf16 v[6:9], v[202:205], v[194:197], v[6:9]
	v_mfma_f32_16x16x32_bf16 v[2:5], v[210:213], v[194:197], v[2:5]
	v_mfma_f32_16x16x32_bf16 v[54:57], v[206:209], v[170:173], v[54:57]
	v_mfma_f32_16x16x32_bf16 v[50:53], v[214:217], v[170:173], v[50:53]
	v_mfma_f32_16x16x32_bf16 v[38:41], v[206:209], v[178:181], v[38:41]
	v_mfma_f32_16x16x32_bf16 v[34:37], v[214:217], v[178:181], v[34:37]
	v_mfma_f32_16x16x32_bf16 v[22:25], v[206:209], v[186:189], v[22:25]
	v_mfma_f32_16x16x32_bf16 v[18:21], v[214:217], v[186:189], v[18:21]
	v_mfma_f32_16x16x32_bf16 v[6:9], v[206:209], v[198:201], v[6:9]
	v_mfma_f32_16x16x32_bf16 v[2:5], v[214:217], v[198:201], v[2:5]
	s_setprio 0
	s_add_i32 s59, s59, 2
	s_add_u32 s20, s20, 0x100
	s_addc_u32 s21, s21, 0
	s_add_u32 s57, s57, 0x100
	s_addc_u32 s58, s58, 0
	s_cmpk_gt_u32 s59, 0x55
	s_barrier
	s_cbranch_scc0 .LBB0_2043
	s_lshl_b32 s20, s55, 8
	v_mbcnt_lo_u32_b32 v130, -1, 0
	v_mbcnt_hi_u32_b32 v130, -1, v130
	s_add_i32 s20, s20, s43
	s_lshl_b32 s21, s56, 8
	v_ashrrev_i32_e32 v131, 2, v130
	s_or_b32 s21, s21, s44
	v_and_b32_e32 v131, -4, v131
	v_and_or_b32 v168, v130, 15, s20
	v_add_u32_e32 v166, s21, v131
	v_ashrrev_i32_e32 v169, 31, v168
	v_ashrrev_i32_e32 v167, 31, v166
	v_lshlrev_b64 v[130:131], 11, v[168:169]
	v_lshl_add_u64 v[130:131], v[130:131], 0, v[166:167]
	v_lshlrev_b64 v[130:131], 2, v[130:131]
	v_lshl_add_u64 v[162:163], s[4:5], 0, v[130:131]
	s_and_b64 vcc, exec, s[14:15]
	s_mov_b32 s56, s54
	s_mov_b32 s55, s53
	s_mov_b64 s[22:23], s[18:19]
	s_mov_b64 s[20:21], s[16:17]
	s_waitcnt lgkmcnt(0)
	v_or_b32_e32 v244, 16, v168
	v_ashrrev_i32_e32 v245, 31, v244
	v_lshlrev_b64 v[244:245], 11, v[244:245]
	v_lshl_add_u64 v[244:245], v[244:245], 0, v[166:167]
	v_lshlrev_b64 v[244:245], 2, v[244:245]
	v_or_b32_e32 v246, 32, v168
	v_ashrrev_i32_e32 v247, 31, v246
	v_lshlrev_b64 v[246:247], 11, v[246:247]
	v_lshl_add_u64 v[246:247], v[246:247], 0, v[166:167]
	v_lshlrev_b64 v[246:247], 2, v[246:247]
	v_or_b32_e32 v248, 48, v168
	v_ashrrev_i32_e32 v249, 31, v248
	v_lshlrev_b64 v[248:249], 11, v[248:249]
	v_lshl_add_u64 v[248:249], v[248:249], 0, v[166:167]
	v_lshlrev_b64 v[248:249], 2, v[248:249]
	v_lshl_add_u64 v[250:251], s[4:5], 0, v[130:131]
	global_load_dwordx4 v[150:153], v[250:251], off
	global_load_dwordx4 v[154:157], v[250:251], off offset:64
	global_load_dwordx4 v[158:161], v[250:251], off offset:512
	global_load_dwordx4 v[162:165], v[250:251], off offset:576
	v_lshl_add_u64 v[250:251], s[4:5], 0, v[244:245]
	global_load_dwordx4 v[170:173], v[250:251], off
	global_load_dwordx4 v[174:177], v[250:251], off offset:64
	global_load_dwordx4 v[178:181], v[250:251], off offset:512
	global_load_dwordx4 v[182:185], v[250:251], off offset:576
	v_lshl_add_u64 v[250:251], s[4:5], 0, v[246:247]
	global_load_dwordx4 v[186:189], v[250:251], off
	global_load_dwordx4 v[194:197], v[250:251], off offset:64
	global_load_dwordx4 v[198:201], v[250:251], off offset:512
	global_load_dwordx4 v[202:205], v[250:251], off offset:576
	v_lshl_add_u64 v[250:251], s[4:5], 0, v[248:249]
	global_load_dwordx4 v[206:209], v[250:251], off
	global_load_dwordx4 v[210:213], v[250:251], off offset:64
	global_load_dwordx4 v[214:217], v[250:251], off offset:512
	global_load_dwordx4 v[252:255], v[250:251], off offset:576
	s_waitcnt vmcnt(0)
;     __device__ __forceinline__ void operator()(const f32x4 (&acc)[2][2][4][2], const Unit& u, int wr, int wc, int fr, int fq) const {
;     ...
;             for (int m = 0; m < 4; ++m) { const size_t off = (size_t)(row0 + ai * HALF + m * 16) * ldc + col0;
; #pragma unroll
;                 for (int bj = 0; bj < 2; ++bj)
; #pragma unroll
;                     for (int n = 0; n < 2; ++n) { f32x4 v = acc[ai][bj][m][n] * cs[bj][n];
;                         if (res) v += *(const f32x4*)(res + off + bj * HALF + n * 16);
;                         *(f32x4*)(out + off + bj * HALF + n * 16) = v; }
;                 asm volatile("" ::: "memory"); }
	v_pk_add_f32 v[126:127], v[126:127], v[150:151]
	v_pk_add_f32 v[128:129], v[128:129], v[152:153]
	v_pk_add_f32 v[122:123], v[122:123], v[154:155]
	v_pk_add_f32 v[124:125], v[124:125], v[156:157]
	v_pk_add_f32 v[118:119], v[118:119], v[158:159]
	v_pk_add_f32 v[120:121], v[120:121], v[160:161]
	v_pk_add_f32 v[114:115], v[114:115], v[162:163]
	v_pk_add_f32 v[116:117], v[116:117], v[164:165]
	v_lshl_add_u64 v[150:151], s[6:7], 0, v[130:131]
	global_store_dwordx4 v[150:151], v[126:129], off
	global_store_dwordx4 v[150:151], v[122:125], off offset:64
	global_store_dwordx4 v[150:151], v[118:121], off offset:512
	global_store_dwordx4 v[150:151], v[114:117], off offset:576
	v_pk_add_f32 v[110:111], v[110:111], v[170:171]
	v_pk_add_f32 v[112:113], v[112:113], v[172:173]
	v_pk_add_f32 v[106:107], v[106:107], v[174:175]
	v_pk_add_f32 v[108:109], v[108:109], v[176:177]
	v_pk_add_f32 v[102:103], v[102:103], v[178:179]
	v_pk_add_f32 v[104:105], v[104:105], v[180:181]
	v_pk_add_f32 v[98:99], v[98:99], v[182:183]
	v_pk_add_f32 v[100:101], v[100:101], v[184:185]
	v_lshl_add_u64 v[170:171], s[6:7], 0, v[244:245]
	global_store_dwordx4 v[170:171], v[110:113], off
	global_store_dwordx4 v[170:171], v[106:109], off offset:64
	global_store_dwordx4 v[170:171], v[102:105], off offset:512
	global_store_dwordx4 v[170:171], v[98:101], off offset:576
	v_pk_add_f32 v[94:95], v[94:95], v[186:187]
	v_pk_add_f32 v[96:97], v[96:97], v[188:189]
	v_pk_add_f32 v[90:91], v[90:91], v[194:195]
	v_pk_add_f32 v[92:93], v[92:93], v[196:197]
	v_pk_add_f32 v[86:87], v[86:87], v[198:199]
	v_pk_add_f32 v[88:89], v[88:89], v[200:201]
	v_pk_add_f32 v[82:83], v[82:83], v[202:203]
	v_pk_add_f32 v[84:85], v[84:85], v[204:205]
	v_lshl_add_u64 v[186:187], s[6:7], 0, v[246:247]
	global_store_dwordx4 v[186:187], v[94:97], off
	global_store_dwordx4 v[186:187], v[90:93], off offset:64
	global_store_dwordx4 v[186:187], v[86:89], off offset:512
	global_store_dwordx4 v[186:187], v[82:85], off offset:576
	v_pk_add_f32 v[78:79], v[78:79], v[206:207]
	v_pk_add_f32 v[80:81], v[80:81], v[208:209]
	v_pk_add_f32 v[74:75], v[74:75], v[210:211]
	v_pk_add_f32 v[76:77], v[76:77], v[212:213]
	v_pk_add_f32 v[70:71], v[70:71], v[214:215]
	v_pk_add_f32 v[72:73], v[72:73], v[216:217]
	v_pk_add_f32 v[66:67], v[66:67], v[252:253]
	v_pk_add_f32 v[68:69], v[68:69], v[254:255]
	v_lshl_add_u64 v[206:207], s[6:7], 0, v[248:249]
	global_store_dwordx4 v[206:207], v[78:81], off
	global_store_dwordx4 v[206:207], v[74:77], off offset:64
	global_store_dwordx4 v[206:207], v[70:73], off offset:512
	global_store_dwordx4 v[206:207], v[66:69], off offset:576
	v_lshl_add_u64 v[130:131], v[130:131], 0, s[8:9]
	v_lshl_add_u64 v[244:245], v[244:245], 0, s[8:9]
	v_lshl_add_u64 v[246:247], v[246:247], 0, s[8:9]
	v_lshl_add_u64 v[248:249], v[248:249], 0, s[8:9]
	v_lshl_add_u64 v[250:251], s[4:5], 0, v[130:131]
	global_load_dwordx4 v[150:153], v[250:251], off
	global_load_dwordx4 v[154:157], v[250:251], off offset:64
	global_load_dwordx4 v[158:161], v[250:251], off offset:512
	global_load_dwordx4 v[162:165], v[250:251], off offset:576
	v_lshl_add_u64 v[250:251], s[4:5], 0, v[244:245]
	global_load_dwordx4 v[170:173], v[250:251], off
	global_load_dwordx4 v[174:177], v[250:251], off offset:64
	global_load_dwordx4 v[178:181], v[250:251], off offset:512
	global_load_dwordx4 v[182:185], v[250:251], off offset:576
	v_lshl_add_u64 v[250:251], s[4:5], 0, v[246:247]
	global_load_dwordx4 v[186:189], v[250:251], off
	global_load_dwordx4 v[194:197], v[250:251], off offset:64
	global_load_dwordx4 v[198:201], v[250:251], off offset:512
	global_load_dwordx4 v[202:205], v[250:251], off offset:576
	v_lshl_add_u64 v[250:251], s[4:5], 0, v[248:249]
	global_load_dwordx4 v[206:209], v[250:251], off
	global_load_dwordx4 v[210:213], v[250:251], off offset:64
	global_load_dwordx4 v[214:217], v[250:251], off offset:512
	global_load_dwordx4 v[252:255], v[250:251], off offset:576
	s_waitcnt vmcnt(0)
	v_pk_add_f32 v[62:63], v[62:63], v[150:151]
	v_pk_add_f32 v[64:65], v[64:65], v[152:153]
	v_pk_add_f32 v[58:59], v[58:59], v[154:155]
	v_pk_add_f32 v[60:61], v[60:61], v[156:157]
	v_pk_add_f32 v[54:55], v[54:55], v[158:159]
	v_pk_add_f32 v[56:57], v[56:57], v[160:161]
	v_pk_add_f32 v[50:51], v[50:51], v[162:163]
	v_pk_add_f32 v[52:53], v[52:53], v[164:165]
	v_lshl_add_u64 v[150:151], s[6:7], 0, v[130:131]
	global_store_dwordx4 v[150:151], v[62:65], off
	global_store_dwordx4 v[150:151], v[58:61], off offset:64
	global_store_dwordx4 v[150:151], v[54:57], off offset:512
	global_store_dwordx4 v[150:151], v[50:53], off offset:576
	v_pk_add_f32 v[46:47], v[46:47], v[170:171]
	v_pk_add_f32 v[48:49], v[48:49], v[172:173]
	v_pk_add_f32 v[42:43], v[42:43], v[174:175]
	v_pk_add_f32 v[44:45], v[44:45], v[176:177]
	v_pk_add_f32 v[38:39], v[38:39], v[178:179]
	v_pk_add_f32 v[40:41], v[40:41], v[180:181]
	v_pk_add_f32 v[34:35], v[34:35], v[182:183]
	v_pk_add_f32 v[36:37], v[36:37], v[184:185]
	v_lshl_add_u64 v[170:171], s[6:7], 0, v[244:245]
	global_store_dwordx4 v[170:171], v[46:49], off
	global_store_dwordx4 v[170:171], v[42:45], off offset:64
	global_store_dwordx4 v[170:171], v[38:41], off offset:512
	global_store_dwordx4 v[170:171], v[34:37], off offset:576
	v_pk_add_f32 v[30:31], v[30:31], v[186:187]
	v_pk_add_f32 v[32:33], v[32:33], v[188:189]
	v_pk_add_f32 v[26:27], v[26:27], v[194:195]
	v_pk_add_f32 v[28:29], v[28:29], v[196:197]
	v_pk_add_f32 v[22:23], v[22:23], v[198:199]
	v_pk_add_f32 v[24:25], v[24:25], v[200:201]
	v_pk_add_f32 v[18:19], v[18:19], v[202:203]
	v_pk_add_f32 v[20:21], v[20:21], v[204:205]
	v_lshl_add_u64 v[186:187], s[6:7], 0, v[246:247]
	global_store_dwordx4 v[186:187], v[30:33], off
	global_store_dwordx4 v[186:187], v[26:29], off offset:64
	global_store_dwordx4 v[186:187], v[22:25], off offset:512
	global_store_dwordx4 v[186:187], v[18:21], off offset:576
	v_pk_add_f32 v[14:15], v[14:15], v[206:207]
	v_pk_add_f32 v[16:17], v[16:17], v[208:209]
	v_pk_add_f32 v[10:11], v[10:11], v[210:211]
	v_pk_add_f32 v[12:13], v[12:13], v[212:213]
	v_pk_add_f32 v[6:7], v[6:7], v[214:215]
	v_pk_add_f32 v[8:9], v[8:9], v[216:217]
	v_pk_add_f32 v[2:3], v[2:3], v[252:253]
	v_pk_add_f32 v[4:5], v[4:5], v[254:255]
	v_lshl_add_u64 v[206:207], s[6:7], 0, v[248:249]
	global_store_dwordx4 v[206:207], v[14:17], off
	global_store_dwordx4 v[206:207], v[10:13], off offset:64
	global_store_dwordx4 v[206:207], v[6:9], off offset:512
	global_store_dwordx4 v[206:207], v[2:5], off offset:576
	s_cbranch_vccz .LBB0_2036
	s_waitcnt vmcnt(0)
	s_cmpk_gt_u32 s28, 0xff
	s_cbranch_scc1 .LBB0_2047
	s_barrier

;     __device__ __forceinline__ void operator()(const f32x4 (&acc)[2][2][4][2], const Unit& u, int wr, int wc, int fr, int fq) const {
;     ...
;             for (int n = 0; n < 2; ++n) cs[bj][n] = (cscale ? *(const f32x4*)(cscale + col0 + bj * HALF + n * 16) : (f32x4){1.f, 1.f, 1.f, 1.f}) * ascale;
; #pragma unroll
;         for (int ai = 0; ai < 2; ++ai)
; #pragma unroll
;             for (int m = 0; m < 4; ++m) { const size_t off = (size_t)(row0 + ai * HALF + m * 16) * ldc + col0;
; #pragma unroll
;                 for (int bj = 0; bj < 2; ++bj)
; #pragma unroll
;                     for (int n = 0; n < 2; ++n) { f32x4 v = acc[ai][bj][m][n] * cs[bj][n];
;                         if (res) v += *(const f32x4*)(res + off + bj * HALF + n * 16);
;                         *(f32x4*)(out + off + bj * HALF + n * 16) = v; }
;                 asm volatile("" ::: "memory"); }
.LBB0_2324:
	s_lshl_b32 s0, s26, 8
	s_add_i32 s0, s0, s50
	v_and_or_b32 v184, v167, 15, s0
	v_ashrrev_i32_e32 v185, 31, v184
	v_lshlrev_b64 v[146:147], 11, v[184:185]
	v_lshl_add_u64 v[146:147], v[146:147], 0, v[148:149]
	v_lshlrev_b64 v[146:147], 2, v[146:147]
	v_lshl_add_u64 v[180:181], s[4:5], 0, v[146:147]
	s_and_b64 vcc, exec, s[18:19]
	s_mov_b32 s61, s60
	s_mov_b32 s26, s20
	s_mov_b64 s[28:29], s[24:25]
	s_mov_b64 s[0:1], s[22:23]
	s_waitcnt lgkmcnt(0)
	v_or_b32_e32 v250, 16, v184
	v_ashrrev_i32_e32 v251, 31, v250
	v_lshlrev_b64 v[250:251], 11, v[250:251]
	v_lshl_add_u64 v[250:251], v[250:251], 0, v[148:149]
	v_lshlrev_b64 v[250:251], 2, v[250:251]
	v_or_b32_e32 v252, 32, v184
	v_ashrrev_i32_e32 v253, 31, v252
	v_lshlrev_b64 v[252:253], 11, v[252:253]
	v_lshl_add_u64 v[252:253], v[252:253], 0, v[148:149]
	v_lshlrev_b64 v[252:253], 2, v[252:253]
	v_or_b32_e32 v254, 48, v184
	v_ashrrev_i32_e32 v255, 31, v254
	v_lshlrev_b64 v[254:255], 11, v[254:255]
	v_lshl_add_u64 v[254:255], v[254:255], 0, v[148:149]
	v_lshlrev_b64 v[254:255], 2, v[254:255]
	v_lshl_add_u64 v[186:187], s[4:5], 0, v[146:147]
	global_load_dwordx4 v[168:171], v[186:187], off
	global_load_dwordx4 v[172:175], v[186:187], off offset:64
	global_load_dwordx4 v[176:179], v[186:187], off offset:512
	global_load_dwordx4 v[180:183], v[186:187], off offset:576
	v_lshl_add_u64 v[186:187], s[4:5], 0, v[250:251]
	global_load_dwordx4 v[194:197], v[186:187], off
	global_load_dwordx4 v[198:201], v[186:187], off offset:64
	global_load_dwordx4 v[202:205], v[186:187], off offset:512
	global_load_dwordx4 v[206:209], v[186:187], off offset:576
	v_lshl_add_u64 v[186:187], s[4:5], 0, v[252:253]
	global_load_dwordx4 v[210:213], v[186:187], off
	global_load_dwordx4 v[214:217], v[186:187], off offset:64
	global_load_dwordx4 v[242:245], v[186:187], off offset:512
	global_load_dwordx4 v[246:249], v[186:187], off offset:576
	s_waitcnt vmcnt(0)
	v_pk_fma_f32 v[126:127], v[126:127], v[134:135], v[168:169]
	v_pk_fma_f32 v[128:129], v[128:129], v[136:137], v[170:171]
	v_pk_fma_f32 v[122:123], v[122:123], v[130:131], v[172:173]
	v_pk_fma_f32 v[124:125], v[124:125], v[132:133], v[174:175]
	v_pk_fma_f32 v[118:119], v[118:119], v[142:143], v[176:177]
	v_pk_fma_f32 v[120:121], v[120:121], v[144:145], v[178:179]
	v_pk_fma_f32 v[114:115], v[114:115], v[138:139], v[180:181]
	v_pk_fma_f32 v[116:117], v[116:117], v[140:141], v[182:183]
	v_lshl_add_u64 v[168:169], s[6:7], 0, v[146:147]
	global_store_dwordx4 v[168:169], v[126:129], off
	global_store_dwordx4 v[168:169], v[122:125], off offset:64
	global_store_dwordx4 v[168:169], v[118:121], off offset:512
	global_store_dwordx4 v[168:169], v[114:117], off offset:576
	v_pk_fma_f32 v[110:111], v[110:111], v[134:135], v[194:195]
	v_pk_fma_f32 v[112:113], v[112:113], v[136:137], v[196:197]
	v_pk_fma_f32 v[106:107], v[106:107], v[130:131], v[198:199]
	v_pk_fma_f32 v[108:109], v[108:109], v[132:133], v[200:201]
	v_pk_fma_f32 v[102:103], v[102:103], v[142:143], v[202:203]
	v_pk_fma_f32 v[104:105], v[104:105], v[144:145], v[204:205]
	v_pk_fma_f32 v[98:99], v[98:99], v[138:139], v[206:207]
	v_pk_fma_f32 v[100:101], v[100:101], v[140:141], v[208:209]
	v_lshl_add_u64 v[194:195], s[6:7], 0, v[250:251]
	global_store_dwordx4 v[194:195], v[110:113], off
	global_store_dwordx4 v[194:195], v[106:109], off offset:64
	global_store_dwordx4 v[194:195], v[102:105], off offset:512
	global_store_dwordx4 v[194:195], v[98:101], off offset:576
	v_pk_fma_f32 v[94:95], v[94:95], v[134:135], v[210:211]
	v_pk_fma_f32 v[96:97], v[96:97], v[136:137], v[212:213]
	v_pk_fma_f32 v[90:91], v[90:91], v[130:131], v[214:215]
	v_pk_fma_f32 v[92:93], v[92:93], v[132:133], v[216:217]
	v_pk_fma_f32 v[86:87], v[86:87], v[142:143], v[242:243]
	v_pk_fma_f32 v[88:89], v[88:89], v[144:145], v[244:245]
	v_pk_fma_f32 v[82:83], v[82:83], v[138:139], v[246:247]
	v_pk_fma_f32 v[84:85], v[84:85], v[140:141], v[248:249]
	v_lshl_add_u64 v[210:211], s[6:7], 0, v[252:253]
	global_store_dwordx4 v[210:211], v[94:97], off
	global_store_dwordx4 v[210:211], v[90:93], off offset:64
	global_store_dwordx4 v[210:211], v[86:89], off offset:512
	global_store_dwordx4 v[210:211], v[82:85], off offset:576
	v_lshl_add_u64 v[186:187], s[4:5], 0, v[254:255]
	global_load_dwordx4 v[168:171], v[186:187], off
	global_load_dwordx4 v[172:175], v[186:187], off offset:64
	global_load_dwordx4 v[176:179], v[186:187], off offset:512
	global_load_dwordx4 v[180:183], v[186:187], off offset:576
	v_lshl_add_u64 v[186:187], s[4:5], 0, v[146:147]
	v_lshl_add_u64 v[186:187], v[186:187], 0, s[10:11]
	global_load_dwordx4 v[194:197], v[186:187], off
	global_load_dwordx4 v[198:201], v[186:187], off offset:64
	global_load_dwordx4 v[202:205], v[186:187], off offset:512
	global_load_dwordx4 v[206:209], v[186:187], off offset:576
	v_lshl_add_u64 v[186:187], s[4:5], 0, v[250:251]
	v_lshl_add_u64 v[186:187], v[186:187], 0, s[10:11]
	global_load_dwordx4 v[210:213], v[186:187], off
	global_load_dwordx4 v[214:217], v[186:187], off offset:64
	global_load_dwordx4 v[242:245], v[186:187], off offset:512
	global_load_dwordx4 v[246:249], v[186:187], off offset:576
	s_waitcnt vmcnt(0)
;     __device__ __forceinline__ void operator()(const f32x4 (&acc)[2][2][4][2], const Unit& u, int wr, int wc, int fr, int fq) const {
;     ...
;             for (int n = 0; n < 2; ++n) cs[bj][n] = (cscale ? *(const f32x4*)(cscale + col0 + bj * HALF + n * 16) : (f32x4){1.f, 1.f, 1.f, 1.f}) * ascale;
; #pragma unroll
;         for (int ai = 0; ai < 2; ++ai)
; #pragma unroll
;             for (int m = 0; m < 4; ++m) { const size_t off = (size_t)(row0 + ai * HALF + m * 16) * ldc + col0;
; #pragma unroll
;                 for (int bj = 0; bj < 2; ++bj)
; #pragma unroll
;                     for (int n = 0; n < 2; ++n) { f32x4 v = acc[ai][bj][m][n] * cs[bj][n];
;                         if (res) v += *(const f32x4*)(res + off + bj * HALF + n * 16);
;                         *(f32x4*)(out + off + bj * HALF + n * 16) = v; }
;                 asm volatile("" ::: "memory"); }
	v_pk_fma_f32 v[78:79], v[78:79], v[134:135], v[168:169]
	v_pk_fma_f32 v[80:81], v[80:81], v[136:137], v[170:171]
	v_pk_fma_f32 v[74:75], v[74:75], v[130:131], v[172:173]
	v_pk_fma_f32 v[76:77], v[76:77], v[132:133], v[174:175]
	v_pk_fma_f32 v[70:71], v[70:71], v[142:143], v[176:177]
	v_pk_fma_f32 v[72:73], v[72:73], v[144:145], v[178:179]
	v_pk_fma_f32 v[66:67], v[66:67], v[138:139], v[180:181]
	v_pk_fma_f32 v[68:69], v[68:69], v[140:141], v[182:183]
	v_lshl_add_u64 v[168:169], s[6:7], 0, v[254:255]
	global_store_dwordx4 v[168:169], v[78:81], off
	global_store_dwordx4 v[168:169], v[74:77], off offset:64
	global_store_dwordx4 v[168:169], v[70:73], off offset:512
	global_store_dwordx4 v[168:169], v[66:69], off offset:576
	v_pk_fma_f32 v[62:63], v[62:63], v[134:135], v[194:195]
	v_pk_fma_f32 v[64:65], v[64:65], v[136:137], v[196:197]
	v_pk_fma_f32 v[58:59], v[58:59], v[130:131], v[198:199]
	v_pk_fma_f32 v[60:61], v[60:61], v[132:133], v[200:201]
	v_pk_fma_f32 v[54:55], v[54:55], v[142:143], v[202:203]
	v_pk_fma_f32 v[56:57], v[56:57], v[144:145], v[204:205]
	v_pk_fma_f32 v[50:51], v[50:51], v[138:139], v[206:207]
	v_pk_fma_f32 v[52:53], v[52:53], v[140:141], v[208:209]
	v_lshl_add_u64 v[194:195], s[6:7], 0, v[146:147]
	v_lshl_add_u64 v[194:195], v[194:195], 0, s[10:11]
	global_store_dwordx4 v[194:195], v[62:65], off
	global_store_dwordx4 v[194:195], v[58:61], off offset:64
	global_store_dwordx4 v[194:195], v[54:57], off offset:512
	global_store_dwordx4 v[194:195], v[50:53], off offset:576
	v_pk_fma_f32 v[46:47], v[46:47], v[134:135], v[210:211]
	v_pk_fma_f32 v[48:49], v[48:49], v[136:137], v[212:213]
	v_pk_fma_f32 v[42:43], v[42:43], v[130:131], v[214:215]
	v_pk_fma_f32 v[44:45], v[44:45], v[132:133], v[216:217]
	v_pk_fma_f32 v[38:39], v[38:39], v[142:143], v[242:243]
	v_pk_fma_f32 v[40:41], v[40:41], v[144:145], v[244:245]
	v_pk_fma_f32 v[34:35], v[34:35], v[138:139], v[246:247]
	v_pk_fma_f32 v[36:37], v[36:37], v[140:141], v[248:249]
	v_lshl_add_u64 v[210:211], s[6:7], 0, v[250:251]
	v_lshl_add_u64 v[210:211], v[210:211], 0, s[10:11]
	global_store_dwordx4 v[210:211], v[46:49], off
	global_store_dwordx4 v[210:211], v[42:45], off offset:64
	global_store_dwordx4 v[210:211], v[38:41], off offset:512
	global_store_dwordx4 v[210:211], v[34:37], off offset:576
	v_lshl_add_u64 v[186:187], s[4:5], 0, v[252:253]
	v_lshl_add_u64 v[186:187], v[186:187], 0, s[10:11]
	global_load_dwordx4 v[168:171], v[186:187], off
	global_load_dwordx4 v[172:175], v[186:187], off offset:64
	global_load_dwordx4 v[176:179], v[186:187], off offset:512
	global_load_dwordx4 v[180:183], v[186:187], off offset:576
	v_lshl_add_u64 v[186:187], s[4:5], 0, v[254:255]
	v_lshl_add_u64 v[186:187], v[186:187], 0, s[10:11]
	global_load_dwordx4 v[194:197], v[186:187], off
	global_load_dwordx4 v[198:201], v[186:187], off offset:64
	global_load_dwordx4 v[202:205], v[186:187], off offset:512
	global_load_dwordx4 v[206:209], v[186:187], off offset:576
	s_waitcnt vmcnt(0)
	v_pk_fma_f32 v[30:31], v[30:31], v[134:135], v[168:169]
	v_pk_fma_f32 v[32:33], v[32:33], v[136:137], v[170:171]
	v_pk_fma_f32 v[26:27], v[26:27], v[130:131], v[172:173]
	v_pk_fma_f32 v[28:29], v[28:29], v[132:133], v[174:175]
	v_pk_fma_f32 v[22:23], v[22:23], v[142:143], v[176:177]
	v_pk_fma_f32 v[24:25], v[24:25], v[144:145], v[178:179]
	v_pk_fma_f32 v[18:19], v[18:19], v[138:139], v[180:181]
	v_pk_fma_f32 v[20:21], v[20:21], v[140:141], v[182:183]
	v_lshl_add_u64 v[168:169], s[6:7], 0, v[252:253]
	v_lshl_add_u64 v[168:169], v[168:169], 0, s[10:11]
	global_store_dwordx4 v[168:169], v[30:33], off
	global_store_dwordx4 v[168:169], v[26:29], off offset:64
	global_store_dwordx4 v[168:169], v[22:25], off offset:512
	global_store_dwordx4 v[168:169], v[18:21], off offset:576
	v_pk_fma_f32 v[14:15], v[14:15], v[134:135], v[194:195]
	v_pk_fma_f32 v[16:17], v[16:17], v[136:137], v[196:197]
	v_pk_fma_f32 v[10:11], v[10:11], v[130:131], v[198:199]
	v_pk_fma_f32 v[12:13], v[12:13], v[132:133], v[200:201]
	v_pk_fma_f32 v[6:7], v[6:7], v[142:143], v[202:203]
	v_pk_fma_f32 v[8:9], v[8:9], v[144:145], v[204:205]
	v_pk_fma_f32 v[2:3], v[2:3], v[138:139], v[206:207]
	v_pk_fma_f32 v[4:5], v[4:5], v[140:141], v[208:209]
	v_lshl_add_u64 v[194:195], s[6:7], 0, v[254:255]
	v_lshl_add_u64 v[194:195], v[194:195], 0, s[10:11]
	global_store_dwordx4 v[194:195], v[14:17], off
	global_store_dwordx4 v[194:195], v[10:13], off offset:64
	global_store_dwordx4 v[194:195], v[6:9], off offset:512
	global_store_dwordx4 v[194:195], v[2:5], off offset:576
	s_cbranch_vccnz .LBB0_2341
